# MoE gate/up main K-loop: last two MFMA groups of each tile deferred past the end-of-tile barrier so they run while the next tile's first LDS fragment reads are in flight
# speedup vs baseline: 1.0033x; 1.0033x over previous
.Lrot_m1:
	v_mfma_f32_16x16x32_bf16 v[130:133], v[162:165], v[234:237], v[130:133]
	v_mfma_f32_16x16x32_bf16 v[134:137], v[166:169], v[234:237], v[134:137]
	v_mfma_f32_16x16x32_bf16 v[138:141], v[250:253], v[234:237], v[138:141]
	v_mfma_f32_16x16x32_bf16 v[142:145], v[226:229], v[234:237], v[142:145]
	v_mfma_f32_16x16x32_bf16 v[146:149], v[162:165], v[222:225], v[146:149]
	v_mfma_f32_16x16x32_bf16 v[150:153], v[166:169], v[222:225], v[150:153]
	v_mfma_f32_16x16x32_bf16 v[154:157], v[250:253], v[222:225], v[154:157]
	v_mfma_f32_16x16x32_bf16 v[158:161], v[226:229], v[222:225], v[158:161]
	v_add_u32_e32 v252, s88, v181
	v_add_u32_e32 v250, s88, v183
.Ldef_m1_body:
	ds_read_b64_tr_b16 v[222:223], v246
	ds_read_b64_tr_b16 v[224:225], v246 offset:2048
	ds_read_b64_tr_b16 v[226:227], v250
	ds_read_b64_tr_b16 v[228:229], v250 offset:2048
	ds_read_b128 v[162:165], v247
	ds_read_b128 v[166:169], v247 offset:2048
	ds_read_b64_tr_b16 v[230:231], v252
	ds_read_b64_tr_b16 v[232:233], v252 offset:2048
	ds_read_b64_tr_b16 v[234:235], v254
	ds_read_b64_tr_b16 v[236:237], v254 offset:2048
	s_waitcnt lgkmcnt(5)
	v_mfma_f32_16x16x32_bf16 v[62:65], v[222:225], v[162:165], v[62:65]
	ds_read_b128 v[238:241], v247 offset:4096
	s_and_b32 s88, s39, 0x8000
	s_add_i32 s89, s38, s85
	v_mfma_f32_16x16x32_bf16 v[58:61], v[226:229], v[162:165], v[58:61]
	s_mov_b32 s90, m0
	s_mov_b32 m0, s89
	s_nop 0
	global_load_lds_dwordx4 v221, s[18:19]
	s_mov_b32 m0, s90
	s_waitcnt lgkmcnt(3)
	v_mfma_f32_16x16x32_bf16 v[54:57], v[230:233], v[162:165], v[54:57]
	s_waitcnt lgkmcnt(1)
	v_mfma_f32_16x16x32_bf16 v[42:45], v[234:237], v[162:165], v[42:45]
	v_mfma_f32_16x16x32_bf16 v[50:53], v[222:225], v[166:169], v[50:53]
	ds_read_b128 v[162:165], v247 offset:6144
	s_add_i32 s90, s89, 0x2000
	s_mov_b32 s91, m0
	s_mov_b32 m0, s90
	s_nop 0
	global_load_lds_dwordx4 v220, s[18:19]
	s_mov_b32 m0, s91
	v_mfma_f32_16x16x32_bf16 v[46:49], v[226:229], v[166:169], v[46:49]
	v_mfma_f32_16x16x32_bf16 v[38:41], v[230:233], v[166:169], v[38:41]
	v_mfma_f32_16x16x32_bf16 v[34:37], v[234:237], v[166:169], v[34:37]
	s_waitcnt lgkmcnt(1)
	v_mfma_f32_16x16x32_bf16 v[66:69], v[222:225], v[238:241], v[66:69]
	ds_read_b128 v[166:169], v247 offset:8192
	s_add_i32 s90, s89, 0x4000
	s_mov_b32 s91, m0
	s_mov_b32 m0, s90
	s_nop 0
	global_load_lds_dwordx4 v219, s[18:19]
	s_mov_b32 m0, s91
	v_mfma_f32_16x16x32_bf16 v[70:73], v[226:229], v[238:241], v[70:73]
	v_mfma_f32_16x16x32_bf16 v[74:77], v[230:233], v[238:241], v[74:77]
	v_mfma_f32_16x16x32_bf16 v[78:81], v[234:237], v[238:241], v[78:81]
	s_waitcnt lgkmcnt(1)
	v_mfma_f32_16x16x32_bf16 v[82:85], v[222:225], v[162:165], v[82:85]
	ds_read_b128 v[238:241], v247 offset:10240
	s_addk_i32 s89, 0x6000
	s_mov_b32 s90, m0
	s_mov_b32 m0, s89
	s_nop 0
	global_load_lds_dwordx4 v218, s[18:19]
	s_mov_b32 m0, s90
	v_mfma_f32_16x16x32_bf16 v[86:89], v[226:229], v[162:165], v[86:89]
	v_mfma_f32_16x16x32_bf16 v[90:93], v[230:233], v[162:165], v[90:93]
	v_mfma_f32_16x16x32_bf16 v[94:97], v[234:237], v[162:165], v[94:97]
	ds_read_b128 v[242:245], v247 offset:12288
	ds_read_b64_tr_b16 v[162:163], v246 offset:16384
	ds_read_b64_tr_b16 v[164:165], v246 offset:18432
	s_waitcnt lgkmcnt(4)
	v_mfma_f32_16x16x32_bf16 v[98:101], v[222:225], v[166:169], v[98:101]
	v_mfma_f32_16x16x32_bf16 v[102:105], v[226:229], v[166:169], v[102:105]
	v_mfma_f32_16x16x32_bf16 v[106:109], v[230:233], v[166:169], v[106:109]
	v_mfma_f32_16x16x32_bf16 v[110:113], v[234:237], v[166:169], v[110:113]
	ds_read_b128 v[246:249], v247 offset:14336
	ds_read_b64_tr_b16 v[166:167], v250 offset:16384
	ds_read_b64_tr_b16 v[168:169], v250 offset:18432
	s_waitcnt lgkmcnt(6)
	v_mfma_f32_16x16x32_bf16 v[114:117], v[222:225], v[238:241], v[114:117]
	v_mfma_f32_16x16x32_bf16 v[118:121], v[226:229], v[238:241], v[118:121]
	v_mfma_f32_16x16x32_bf16 v[122:125], v[230:233], v[238:241], v[122:125]
	v_mfma_f32_16x16x32_bf16 v[126:129], v[234:237], v[238:241], v[126:129]
	v_add_u32_e32 v200, s87, v216
	ds_read_b128 v[238:241], v200
	ds_read_b64_tr_b16 v[250:251], v252 offset:16384
	ds_read_b64_tr_b16 v[252:253], v252 offset:18432
	s_waitcnt lgkmcnt(8)
	v_mfma_f32_16x16x32_bf16 v[130:133], v[222:225], v[242:245], v[130:133]
	v_mfma_f32_16x16x32_bf16 v[134:137], v[226:229], v[242:245], v[134:137]
	v_mfma_f32_16x16x32_bf16 v[138:141], v[230:233], v[242:245], v[138:141]
	v_mfma_f32_16x16x32_bf16 v[142:145], v[234:237], v[242:245], v[142:145]
	s_waitcnt lgkmcnt(5)
	v_mfma_f32_16x16x32_bf16 v[146:149], v[222:225], v[246:249], v[146:149]
	v_mfma_f32_16x16x32_bf16 v[150:153], v[226:229], v[246:249], v[150:153]
	ds_read_b128 v[222:225], v200 offset:2048
	ds_read_b64_tr_b16 v[226:227], v254 offset:16384
	ds_read_b64_tr_b16 v[228:229], v254 offset:18432
	v_mfma_f32_16x16x32_bf16 v[154:157], v[230:233], v[246:249], v[154:157]
	v_mfma_f32_16x16x32_bf16 v[158:161], v[234:237], v[246:249], v[158:161]
	ds_read_b128 v[230:233], v200 offset:4096
	s_waitcnt lgkmcnt(6)
	v_mfma_f32_16x16x32_bf16 v[62:65], v[162:165], v[238:241], v[62:65]
	s_add_u32 s87, s83, s2
	s_waitcnt vmcnt(11)
	s_addc_u32 s90, s84, s3
	v_mfma_f32_16x16x32_bf16 v[58:61], v[166:169], v[238:241], v[58:61]
	v_cvt_pk_bf16_f32 v30, v30, v31
	v_cvt_pk_bf16_f32 v31, v32, v33
	v_add_u32_e32 v242, s88, v217
	s_waitcnt lgkmcnt(4)
	v_mfma_f32_16x16x32_bf16 v[54:57], v[250:253], v[238:241], v[54:57]
	s_add_u32 s88, s87, 0x160000
	ds_write_b64 v242, v[30:31]
	s_addc_u32 s89, s90, 0
	s_waitcnt lgkmcnt(2)
	v_mfma_f32_16x16x32_bf16 v[42:45], v[226:229], v[238:241], v[42:45]
	global_load_dwordx4 v[30:33], v199, s[88:89] nt
	v_mfma_f32_16x16x32_bf16 v[50:53], v[162:165], v[222:225], v[50:53]
	ds_read_b128 v[234:237], v200 offset:6144
	s_waitcnt vmcnt(11)
	s_add_u32 s88, s87, 0x18c000
	v_mfma_f32_16x16x32_bf16 v[46:49], v[166:169], v[222:225], v[46:49]
	v_cvt_pk_bf16_f32 v26, v26, v27
	v_cvt_pk_bf16_f32 v27, v28, v29
	ds_write_b64 v242, v[26:27] offset:8192
	v_mfma_f32_16x16x32_bf16 v[38:41], v[250:253], v[222:225], v[38:41]
	s_addc_u32 s89, s90, 0
	global_load_dwordx4 v[26:29], v199, s[88:89] nt
	v_mfma_f32_16x16x32_bf16 v[34:37], v[226:229], v[222:225], v[34:37]
	s_waitcnt lgkmcnt(3)
	v_mfma_f32_16x16x32_bf16 v[66:69], v[162:165], v[230:233], v[66:69]
	ds_read_b128 v[222:225], v200 offset:8192
	s_waitcnt vmcnt(11)
	s_add_u32 s88, s87, 0x1b8000
	v_mfma_f32_16x16x32_bf16 v[70:73], v[166:169], v[230:233], v[70:73]
	v_cvt_pk_bf16_f32 v22, v22, v23
	v_cvt_pk_bf16_f32 v23, v24, v25
	ds_write_b64 v242, v[22:23] offset:16384
	v_mfma_f32_16x16x32_bf16 v[74:77], v[250:253], v[230:233], v[74:77]
	s_addc_u32 s89, s90, 0
	global_load_dwordx4 v[22:25], v199, s[88:89] nt
	v_mfma_f32_16x16x32_bf16 v[78:81], v[226:229], v[230:233], v[78:81]
	s_waitcnt lgkmcnt(3)
	v_mfma_f32_16x16x32_bf16 v[82:85], v[162:165], v[234:237], v[82:85]
	ds_read_b128 v[230:233], v200 offset:10240
	s_waitcnt vmcnt(11)
	s_add_u32 s88, s87, 0x1e4000
	v_mfma_f32_16x16x32_bf16 v[86:89], v[166:169], v[234:237], v[86:89]
	v_cvt_pk_bf16_f32 v18, v18, v19
	v_cvt_pk_bf16_f32 v19, v20, v21
	ds_write_b64 v242, v[18:19] offset:24576
	v_mfma_f32_16x16x32_bf16 v[90:93], v[250:253], v[234:237], v[90:93]
	s_addc_u32 s89, s90, 0
	global_load_dwordx4 v[18:21], v199, s[88:89] nt
	v_mfma_f32_16x16x32_bf16 v[94:97], v[226:229], v[234:237], v[94:97]
	ds_read_b128 v[234:237], v200 offset:12288
	s_waitcnt lgkmcnt(4)
	v_mfma_f32_16x16x32_bf16 v[98:101], v[162:165], v[222:225], v[98:101]
	s_add_u32 s87, s40, s2
	s_waitcnt vmcnt(11)
	s_addc_u32 s90, s41, s3
	v_mfma_f32_16x16x32_bf16 v[102:105], v[166:169], v[222:225], v[102:105]
	v_cvt_pk_bf16_f32 v14, v14, v15
	v_cvt_pk_bf16_f32 v15, v16, v17
	s_add_u32 s88, s87, 0x160000
	v_mfma_f32_16x16x32_bf16 v[106:109], v[250:253], v[222:225], v[106:109]
	ds_write_b64 v242, v[14:15] offset:256
	s_addc_u32 s89, s90, 0
	global_load_dwordx4 v[14:17], v199, s[88:89] nt
	v_mfma_f32_16x16x32_bf16 v[110:113], v[226:229], v[222:225], v[110:113]
	s_waitcnt lgkmcnt(3)
	v_mfma_f32_16x16x32_bf16 v[114:117], v[162:165], v[230:233], v[114:117]
	ds_read_b128 v[222:225], v200 offset:14336
	s_waitcnt vmcnt(11)
	s_add_u32 s88, s87, 0x18c000
	v_mfma_f32_16x16x32_bf16 v[118:121], v[166:169], v[230:233], v[118:121]
	v_cvt_pk_bf16_f32 v10, v10, v11
	v_cvt_pk_bf16_f32 v11, v12, v13
	ds_write_b64 v242, v[10:11] offset:8448
	v_mfma_f32_16x16x32_bf16 v[122:125], v[250:253], v[230:233], v[122:125]
	s_addc_u32 s89, s90, 0
	global_load_dwordx4 v[10:13], v199, s[88:89] nt
	v_mfma_f32_16x16x32_bf16 v[126:129], v[226:229], v[230:233], v[126:129]
	s_waitcnt lgkmcnt(3)
	s_waitcnt vmcnt(11)
	s_add_u32 s88, s87, 0x1b8000
	v_cvt_pk_bf16_f32 v6, v6, v7
	v_cvt_pk_bf16_f32 v7, v8, v9
	ds_write_b64 v242, v[6:7] offset:16640
	s_addc_u32 s89, s90, 0
	global_load_dwordx4 v[6:9], v199, s[88:89] nt
	s_waitcnt lgkmcnt(2)
	s_waitcnt vmcnt(11)
	s_add_u32 s88, s87, 0x1e4000
	v_cvt_pk_bf16_f32 v2, v2, v3
	v_cvt_pk_bf16_f32 v3, v4, v5
	ds_write_b64 v242, v[2:3] offset:24832
	s_addc_u32 s89, s90, 0
	global_load_dwordx4 v[2:5], v199, s[88:89] nt
	s_add_i32 s87, s86, 0x8000
	s_cmp_lg_u32 s86, 0x10000
	s_cselect_b32 s86, s87, 0
	s_add_i32 s87, s85, 0x8000
	s_cmp_lg_u32 s85, 0x10000
	s_cselect_b32 s85, s87, 0
	s_add_u32 s2, s2, 0xb0000
	s_addc_u32 s3, s3, 0
	s_add_i32 s39, s39, 0x8000
	v_add_u32_e32 v218, 0x80, v218
	v_add_u32_e32 v219, 0x80, v219
	v_add_u32_e32 v220, 0x80, v220
	v_add_u32_e32 v221, 0x80, v221
	s_add_i32 s88, s39, 0xffff8000
	s_and_b32 s88, s88, 0x8000
	s_add_i32 s88, s88, 0
	s_add_i32 s87, s86, 0
	s_add_i32 s88, s88, 0x18000
	v_add_u32_e32 v246, s88, v212
	v_add_u32_e32 v247, s87, v215
	v_add_u32_e32 v254, s88, v172
	s_waitcnt lgkmcnt(0)
	s_barrier
	s_cmp_lg_u32 s2, 0x14a0000
	s_cbranch_scc1 .Lrot_m1
	v_mfma_f32_16x16x32_bf16 v[130:133], v[162:165], v[234:237], v[130:133]
	v_mfma_f32_16x16x32_bf16 v[134:137], v[166:169], v[234:237], v[134:137]
	v_mfma_f32_16x16x32_bf16 v[138:141], v[250:253], v[234:237], v[138:141]
	v_mfma_f32_16x16x32_bf16 v[142:145], v[226:229], v[234:237], v[142:145]
	v_mfma_f32_16x16x32_bf16 v[146:149], v[162:165], v[222:225], v[146:149]
	v_mfma_f32_16x16x32_bf16 v[150:153], v[166:169], v[222:225], v[150:153]
	v_mfma_f32_16x16x32_bf16 v[154:157], v[250:253], v[222:225], v[154:157]
	v_mfma_f32_16x16x32_bf16 v[158:161], v[226:229], v[222:225], v[158:161]
	v_add_u32_e32 v200, s52, v212
	v_add_u32_e32 v250, 0, v215
	v_add_u32_e32 v215, s52, v181
	v_add_u32_e32 v251, s52, v172
	v_add_u32_e32 v217, s52, v183
	ds_read_b64_tr_b16 v[162:163], v200
	ds_read_b64_tr_b16 v[164:165], v200 offset:2048
	ds_read_b64_tr_b16 v[166:167], v217
	ds_read_b64_tr_b16 v[168:169], v217 offset:2048
	ds_read_b128 v[218:221], v250
	ds_read_b128 v[222:225], v250 offset:2048
	ds_read_b64_tr_b16 v[226:227], v215
	ds_read_b64_tr_b16 v[228:229], v215 offset:2048
	ds_read_b64_tr_b16 v[230:231], v251
	ds_read_b64_tr_b16 v[232:233], v251 offset:2048
	s_waitcnt lgkmcnt(5)
	v_mfma_f32_16x16x32_bf16 v[62:65], v[162:165], v[218:221], v[62:65]
	ds_read_b128 v[234:237], v250 offset:4096
	v_mfma_f32_16x16x32_bf16 v[58:61], v[166:169], v[218:221], v[58:61]
	s_waitcnt lgkmcnt(3)
	v_mfma_f32_16x16x32_bf16 v[54:57], v[226:229], v[218:221], v[54:57]
	s_waitcnt lgkmcnt(1)
	v_mfma_f32_16x16x32_bf16 v[42:45], v[230:233], v[218:221], v[42:45]
	v_mfma_f32_16x16x32_bf16 v[50:53], v[162:165], v[222:225], v[50:53]
	ds_read_b128 v[218:221], v250 offset:6144
	v_mfma_f32_16x16x32_bf16 v[46:49], v[166:169], v[222:225], v[46:49]
	v_mfma_f32_16x16x32_bf16 v[38:41], v[226:229], v[222:225], v[38:41]
	v_mfma_f32_16x16x32_bf16 v[34:37], v[230:233], v[222:225], v[34:37]
	s_waitcnt lgkmcnt(1)
	v_mfma_f32_16x16x32_bf16 v[66:69], v[162:165], v[234:237], v[66:69]
	ds_read_b128 v[222:225], v250 offset:8192
	v_mfma_f32_16x16x32_bf16 v[70:73], v[166:169], v[234:237], v[70:73]
	v_mfma_f32_16x16x32_bf16 v[74:77], v[226:229], v[234:237], v[74:77]
	v_mfma_f32_16x16x32_bf16 v[78:81], v[230:233], v[234:237], v[78:81]
	s_waitcnt lgkmcnt(1)
	v_mfma_f32_16x16x32_bf16 v[82:85], v[162:165], v[218:221], v[82:85]
	ds_read_b128 v[234:237], v250 offset:10240
	v_mfma_f32_16x16x32_bf16 v[86:89], v[166:169], v[218:221], v[86:89]
	v_mfma_f32_16x16x32_bf16 v[90:93], v[226:229], v[218:221], v[90:93]
	v_mfma_f32_16x16x32_bf16 v[94:97], v[230:233], v[218:221], v[94:97]
	ds_read_b128 v[218:221], v250 offset:12288
	ds_read_b64_tr_b16 v[238:239], v200 offset:16384
	ds_read_b64_tr_b16 v[240:241], v200 offset:18432
	s_waitcnt lgkmcnt(4)
	v_mfma_f32_16x16x32_bf16 v[98:101], v[162:165], v[222:225], v[98:101]
	v_mfma_f32_16x16x32_bf16 v[102:105], v[166:169], v[222:225], v[102:105]
	v_mfma_f32_16x16x32_bf16 v[106:109], v[226:229], v[222:225], v[106:109]
	v_mfma_f32_16x16x32_bf16 v[110:113], v[230:233], v[222:225], v[110:113]
	ds_read_b128 v[222:225], v250 offset:14336
	ds_read_b64_tr_b16 v[242:243], v217 offset:16384
	ds_read_b64_tr_b16 v[244:245], v217 offset:18432
	s_waitcnt lgkmcnt(6)
	v_mfma_f32_16x16x32_bf16 v[114:117], v[162:165], v[234:237], v[114:117]
	v_mfma_f32_16x16x32_bf16 v[118:121], v[166:169], v[234:237], v[118:121]
	v_mfma_f32_16x16x32_bf16 v[122:125], v[226:229], v[234:237], v[122:125]
	v_mfma_f32_16x16x32_bf16 v[126:129], v[230:233], v[234:237], v[126:129]
	v_add_u32_e32 v200, 0, v216
	ds_read_b128 v[234:237], v200
	ds_read_b64_tr_b16 v[246:247], v215 offset:16384
	ds_read_b64_tr_b16 v[248:249], v215 offset:18432
	s_waitcnt lgkmcnt(8)
	v_mfma_f32_16x16x32_bf16 v[130:133], v[162:165], v[218:221], v[130:133]
	v_mfma_f32_16x16x32_bf16 v[134:137], v[166:169], v[218:221], v[134:137]
	v_mfma_f32_16x16x32_bf16 v[138:141], v[226:229], v[218:221], v[138:141]
	v_mfma_f32_16x16x32_bf16 v[142:145], v[230:233], v[218:221], v[142:145]
	s_waitcnt lgkmcnt(5)
	v_mfma_f32_16x16x32_bf16 v[146:149], v[162:165], v[222:225], v[146:149]
	v_mfma_f32_16x16x32_bf16 v[150:153], v[166:169], v[222:225], v[150:153]
	ds_read_b128 v[162:165], v200 offset:2048
	ds_read_b64_tr_b16 v[166:167], v251 offset:16384
	ds_read_b64_tr_b16 v[168:169], v251 offset:18432
	v_mfma_f32_16x16x32_bf16 v[154:157], v[226:229], v[222:225], v[154:157]
	v_mfma_f32_16x16x32_bf16 v[158:161], v[230:233], v[222:225], v[158:161]
	ds_read_b128 v[216:219], v200 offset:4096
	s_waitcnt vmcnt(7)
	v_add_u32_e32 v214, s56, v214
	v_cvt_pk_bf16_f32 v30, v30, v31
	v_cvt_pk_bf16_f32 v31, v32, v33
	s_waitcnt lgkmcnt(6)
	v_mfma_f32_16x16x32_bf16 v[62:65], v[238:241], v[234:237], v[62:65]
	ds_write_b64 v214, v[30:31]
	v_mfma_f32_16x16x32_bf16 v[58:61], v[242:245], v[234:237], v[58:61]
	s_waitcnt lgkmcnt(5)
	v_mfma_f32_16x16x32_bf16 v[54:57], v[246:249], v[234:237], v[54:57]
	s_waitcnt lgkmcnt(2)
	v_mfma_f32_16x16x32_bf16 v[30:33], v[166:169], v[234:237], v[42:45]
	v_mfma_f32_16x16x32_bf16 v[42:45], v[238:241], v[162:165], v[50:53]
	s_nop 2
	ds_read_b128 v[50:53], v200 offset:6144
	s_waitcnt vmcnt(6)
	v_mfma_f32_16x16x32_bf16 v[46:49], v[242:245], v[162:165], v[46:49]
	v_cvt_pk_bf16_f32 v26, v26, v27
	v_cvt_pk_bf16_f32 v27, v28, v29
	ds_write_b64 v214, v[26:27] offset:8192
	v_mfma_f32_16x16x32_bf16 v[38:41], v[246:249], v[162:165], v[38:41]
	v_mfma_f32_16x16x32_bf16 v[26:29], v[166:169], v[162:165], v[34:37]
	s_waitcnt lgkmcnt(3)
	v_mfma_f32_16x16x32_bf16 v[34:37], v[238:241], v[216:219], v[66:69]
	v_mfma_f32_16x16x32_bf16 v[66:69], v[242:245], v[216:219], v[70:73]
	s_nop 2
	ds_read_b128 v[70:73], v200 offset:8192
	s_waitcnt vmcnt(5)
	v_mfma_f32_16x16x32_bf16 v[74:77], v[246:249], v[216:219], v[74:77]
	v_cvt_pk_bf16_f32 v22, v22, v23
	v_cvt_pk_bf16_f32 v23, v24, v25
	ds_write_b64 v214, v[22:23] offset:16384
	v_mfma_f32_16x16x32_bf16 v[22:25], v[166:169], v[216:219], v[78:81]
	s_waitcnt lgkmcnt(3)
	v_mfma_f32_16x16x32_bf16 v[78:81], v[238:241], v[50:53], v[82:85]
	v_mfma_f32_16x16x32_bf16 v[82:85], v[242:245], v[50:53], v[86:89]
	s_nop 2
	ds_read_b128 v[86:89], v200 offset:10240
	s_waitcnt vmcnt(4)
	v_mfma_f32_16x16x32_bf16 v[90:93], v[246:249], v[50:53], v[90:93]
	v_cvt_pk_bf16_f32 v18, v18, v19
	v_cvt_pk_bf16_f32 v19, v20, v21
	ds_write_b64 v214, v[18:19] offset:24576
	v_mfma_f32_16x16x32_bf16 v[18:21], v[166:169], v[50:53], v[94:97]
	s_waitcnt lgkmcnt(3)
	v_mfma_f32_16x16x32_bf16 v[50:53], v[238:241], v[70:73], v[98:101]
	v_add_u32_e32 v162, s56, v213
	s_nop 1
	ds_read_b128 v[98:101], v200 offset:12288
	s_waitcnt vmcnt(3)
	v_mfma_f32_16x16x32_bf16 v[94:97], v[242:245], v[70:73], v[102:105]
	v_cvt_pk_bf16_f32 v14, v14, v15
	v_cvt_pk_bf16_f32 v15, v16, v17
	ds_write_b64 v162, v[14:15]
	v_mfma_f32_16x16x32_bf16 v[102:105], v[246:249], v[70:73], v[106:109]
	v_mfma_f32_16x16x32_bf16 v[14:17], v[166:169], v[70:73], v[110:113]
	s_nop 2
	ds_read_b128 v[110:113], v200 offset:14336
	s_waitcnt vmcnt(2)
	s_waitcnt lgkmcnt(4)
	v_mfma_f32_16x16x32_bf16 v[70:73], v[238:241], v[86:89], v[114:117]
	v_cvt_pk_bf16_f32 v10, v10, v11
	v_cvt_pk_bf16_f32 v11, v12, v13
	ds_write_b64 v162, v[10:11] offset:8192
	v_mfma_f32_16x16x32_bf16 v[106:109], v[242:245], v[86:89], v[118:121]
	v_mfma_f32_16x16x32_bf16 v[114:117], v[246:249], v[86:89], v[122:125]
	v_mfma_f32_16x16x32_bf16 v[10:13], v[166:169], v[86:89], v[126:129]
	s_waitcnt vmcnt(1)
	s_waitcnt lgkmcnt(3)
	v_mfma_f32_16x16x32_bf16 v[86:89], v[238:241], v[98:101], v[130:133]
	v_cvt_pk_bf16_f32 v6, v6, v7
	v_cvt_pk_bf16_f32 v7, v8, v9
	ds_write_b64 v162, v[6:7] offset:16384
	v_mfma_f32_16x16x32_bf16 v[118:121], v[242:245], v[98:101], v[134:137]
	v_mfma_f32_16x16x32_bf16 v[122:125], v[246:249], v[98:101], v[138:141]
	v_mfma_f32_16x16x32_bf16 v[6:9], v[166:169], v[98:101], v[142:145]
	s_waitcnt vmcnt(0)
	s_waitcnt lgkmcnt(2)
	v_mfma_f32_16x16x32_bf16 v[98:101], v[238:241], v[110:113], v[146:149]
	v_cvt_pk_bf16_f32 v2, v2, v3
	v_cvt_pk_bf16_f32 v3, v4, v5
	ds_write_b64 v162, v[2:3] offset:24576
	v_mfma_f32_16x16x32_bf16 v[126:129], v[242:245], v[110:113], v[150:153]
	v_mfma_f32_16x16x32_bf16 v[130:133], v[246:249], v[110:113], v[154:157]
	v_mfma_f32_16x16x32_bf16 v[2:5], v[166:169], v[110:113], v[158:161]
	s_waitcnt lgkmcnt(0)
	s_barrier
	v_add_u32_e32 v168, s56, v212
	v_add_u32_e32 v183, s56, v183
	v_add_u32_e32 v181, s56, v181
	ds_read_b64_tr_b16 v[110:111], v168
	ds_read_b64_tr_b16 v[112:113], v168 offset:2048
	ds_read_b64_tr_b16 v[134:135], v183
	ds_read_b64_tr_b16 v[136:137], v183 offset:2048
	ds_read_b128 v[138:141], v250 offset:32768
	ds_read_b64_tr_b16 v[142:143], v181
	ds_read_b128 v[146:149], v250 offset:34816
	ds_read_b128 v[150:153], v250 offset:36864
	ds_read_b64_tr_b16 v[144:145], v181 offset:2048
	v_add_u32_e32 v172, s56, v172
	ds_read_b64_tr_b16 v[154:155], v172
	ds_read_b64_tr_b16 v[156:157], v172 offset:2048
	s_waitcnt lgkmcnt(6)
	v_mfma_f32_16x16x32_bf16 v[62:65], v[110:113], v[138:141], v[62:65]
	v_mfma_f32_16x16x32_bf16 v[58:61], v[134:137], v[138:141], v[58:61]
	s_waitcnt lgkmcnt(2)
	v_mfma_f32_16x16x32_bf16 v[54:57], v[142:145], v[138:141], v[54:57]
	s_waitcnt lgkmcnt(0)
	v_mfma_f32_16x16x32_bf16 v[30:33], v[154:157], v[138:141], v[30:33]
	v_mfma_f32_16x16x32_bf16 v[42:45], v[110:113], v[146:149], v[42:45]
	ds_read_b128 v[138:141], v250 offset:38912
	v_mfma_f32_16x16x32_bf16 v[46:49], v[134:137], v[146:149], v[46:49]
	v_mfma_f32_16x16x32_bf16 v[38:41], v[142:145], v[146:149], v[38:41]
	v_mfma_f32_16x16x32_bf16 v[26:29], v[154:157], v[146:149], v[26:29]
	v_mfma_f32_16x16x32_bf16 v[34:37], v[110:113], v[150:153], v[34:37]
	ds_read_b128 v[146:149], v250 offset:40960
	v_mfma_f32_16x16x32_bf16 v[66:69], v[134:137], v[150:153], v[66:69]
	v_mfma_f32_16x16x32_bf16 v[74:77], v[142:145], v[150:153], v[74:77]
	v_mfma_f32_16x16x32_bf16 v[22:25], v[154:157], v[150:153], v[22:25]
	s_waitcnt lgkmcnt(1)
	v_mfma_f32_16x16x32_bf16 v[150:153], v[134:137], v[138:141], v[82:85]
	s_nop 2
	ds_read_b128 v[82:85], v250 offset:43008
	v_mfma_f32_16x16x32_bf16 v[78:81], v[110:113], v[138:141], v[78:81]
	v_mfma_f32_16x16x32_bf16 v[18:21], v[154:157], v[138:141], v[18:21]
	v_mfma_f32_16x16x32_bf16 v[158:161], v[142:145], v[138:141], v[90:93]
	s_nop 2
	ds_read_b128 v[90:93], v250 offset:45056
	ds_read_b64_tr_b16 v[166:167], v168 offset:16384
	ds_read_b64_tr_b16 v[168:169], v168 offset:18432
	s_waitcnt lgkmcnt(4)
	v_mfma_f32_16x16x32_bf16 v[50:53], v[110:113], v[146:149], v[50:53]
	v_mfma_f32_16x16x32_bf16 v[14:17], v[154:157], v[146:149], v[14:17]
	v_mfma_f32_16x16x32_bf16 v[138:141], v[134:137], v[146:149], v[94:97]
	v_mfma_f32_16x16x32_bf16 v[162:165], v[142:145], v[146:149], v[102:105]
	s_waitcnt lgkmcnt(3)
	v_mfma_f32_16x16x32_bf16 v[146:149], v[110:113], v[82:85], v[70:73]
	s_nop 2
	ds_read_b128 v[70:73], v250 offset:47104
	ds_read_b64_tr_b16 v[220:221], v183 offset:16384
	ds_read_b64_tr_b16 v[222:223], v183 offset:18432
	v_mfma_f32_16x16x32_bf16 v[10:13], v[154:157], v[82:85], v[10:13]
	v_mfma_f32_16x16x32_bf16 v[212:215], v[134:137], v[82:85], v[106:109]
	v_mfma_f32_16x16x32_bf16 v[216:219], v[142:145], v[82:85], v[114:117]
	ds_read_b128 v[82:85], v200 offset:32768
	ds_read_b64_tr_b16 v[236:237], v181 offset:16384
	ds_read_b64_tr_b16 v[238:239], v181 offset:18432
	s_waitcnt lgkmcnt(8)
	v_mfma_f32_16x16x32_bf16 v[6:9], v[154:157], v[90:93], v[6:9]
	v_mfma_f32_16x16x32_bf16 v[224:227], v[110:113], v[90:93], v[86:89]
	v_mfma_f32_16x16x32_bf16 v[228:231], v[134:137], v[90:93], v[118:121]
	v_mfma_f32_16x16x32_bf16 v[232:235], v[142:145], v[90:93], v[122:125]
	s_waitcnt lgkmcnt(5)
	v_mfma_f32_16x16x32_bf16 v[130:133], v[142:145], v[70:73], v[130:133]
	ds_read_b128 v[86:89], v200 offset:34816
	ds_read_b64_tr_b16 v[142:143], v172 offset:16384
	ds_read_b64_tr_b16 v[144:145], v172 offset:18432
	v_mfma_f32_16x16x32_bf16 v[240:243], v[110:113], v[70:73], v[98:101]
	v_mfma_f32_16x16x32_bf16 v[134:137], v[134:137], v[70:73], v[126:129]
	v_mfma_f32_16x16x32_bf16 v[154:157], v[154:157], v[70:73], v[2:5]
	s_nop 2
	ds_read_b128 v[2:5], v200 offset:36864
	s_waitcnt lgkmcnt(6)
	v_mfma_f32_16x16x32_bf16 v[122:125], v[166:169], v[82:85], v[62:65]
	v_mfma_f32_16x16x32_bf16 v[114:117], v[220:223], v[82:85], v[58:61]
	s_waitcnt lgkmcnt(4)
	v_mfma_f32_16x16x32_bf16 v[126:129], v[236:239], v[82:85], v[54:57]
	s_waitcnt lgkmcnt(1)
	v_mfma_f32_16x16x32_bf16 v[118:121], v[142:145], v[82:85], v[30:33]
	s_nop 2
	ds_read_b128 v[30:33], v200 offset:38912
	v_mfma_f32_16x16x32_bf16 v[106:109], v[166:169], v[86:89], v[42:45]
	v_mfma_f32_16x16x32_bf16 v[98:101], v[220:223], v[86:89], v[46:49]
	v_mfma_f32_16x16x32_bf16 v[110:113], v[236:239], v[86:89], v[38:41]
	v_mfma_f32_16x16x32_bf16 v[102:105], v[142:145], v[86:89], v[26:29]
	s_nop 2
	ds_read_b128 v[26:29], v200 offset:40960
	s_waitcnt lgkmcnt(2)
	v_mfma_f32_16x16x32_bf16 v[90:93], v[166:169], v[2:5], v[34:37]
	v_mfma_f32_16x16x32_bf16 v[82:85], v[220:223], v[2:5], v[66:69]
	v_mfma_f32_16x16x32_bf16 v[94:97], v[236:239], v[2:5], v[74:77]
	v_mfma_f32_16x16x32_bf16 v[86:89], v[142:145], v[2:5], v[22:25]
	ds_read_b128 v[2:5], v200 offset:43008
	s_waitcnt lgkmcnt(2)
	v_mfma_f32_16x16x32_bf16 v[74:77], v[166:169], v[30:33], v[78:81]
	v_mfma_f32_16x16x32_bf16 v[66:69], v[220:223], v[30:33], v[150:153]
	v_mfma_f32_16x16x32_bf16 v[78:81], v[236:239], v[30:33], v[158:161]
	v_mfma_f32_16x16x32_bf16 v[70:73], v[142:145], v[30:33], v[18:21]
	ds_read_b128 v[22:25], v200 offset:45056
	s_waitcnt lgkmcnt(2)
	v_mfma_f32_16x16x32_bf16 v[58:61], v[166:169], v[26:29], v[50:53]
	v_mfma_f32_16x16x32_bf16 v[50:53], v[220:223], v[26:29], v[138:141]
	v_mfma_f32_16x16x32_bf16 v[62:65], v[236:239], v[26:29], v[162:165]
	v_mfma_f32_16x16x32_bf16 v[54:57], v[142:145], v[26:29], v[14:17]
	s_waitcnt lgkmcnt(1)
	v_mfma_f32_16x16x32_bf16 v[42:45], v[166:169], v[2:5], v[146:149]
	ds_read_b128 v[138:141], v200 offset:47104
	v_mfma_f32_16x16x32_bf16 v[34:37], v[220:223], v[2:5], v[212:215]
	v_mfma_f32_16x16x32_bf16 v[46:49], v[236:239], v[2:5], v[216:219]
	v_mfma_f32_16x16x32_bf16 v[38:41], v[142:145], v[2:5], v[10:13]
	s_waitcnt lgkmcnt(1)
	v_mfma_f32_16x16x32_bf16 v[26:29], v[166:169], v[22:25], v[224:227]
	v_mfma_f32_16x16x32_bf16 v[18:21], v[220:223], v[22:25], v[228:231]
	v_mfma_f32_16x16x32_bf16 v[30:33], v[236:239], v[22:25], v[232:235]
	v_mfma_f32_16x16x32_bf16 v[22:25], v[142:145], v[22:25], v[6:9]
	s_waitcnt lgkmcnt(0)
	v_mfma_f32_16x16x32_bf16 v[10:13], v[166:169], v[138:141], v[240:243]
	v_mfma_f32_16x16x32_bf16 v[2:5], v[220:223], v[138:141], v[134:137]
	v_mfma_f32_16x16x32_bf16 v[14:17], v[236:239], v[138:141], v[130:133]
	v_mfma_f32_16x16x32_bf16 v[6:9], v[142:145], v[138:141], v[154:157]
	s_waitcnt lgkmcnt(0)
	s_barrier
	s_nop 0
	v_mov_b32_e32 v130, 0
	s_and_b64 vcc, exec, s[6:7]
	v_mov_b32_e32 v131, 0
	v_mov_b32_e32 v132, 0
	s_cbranch_vccnz .LBB0_1436
	global_load_dword v130, v[184:185], off
	global_load_dword v131, v[186:187], off
	global_load_dword v132, v[188:189], off
